# conversion slots between attention units take 4 items per wave instead of 3 (queue empties inside the slots, shorter closing drain); 8 sub-queues, 4 per claim
# baseline (speedup 1.0000x reference)
; #define LAS __attribute__((address_space(3)))
; #define LDS_WAIT() asm volatile("s_waitcnt lgkmcnt(0)" ::: "memory")
; #define RI_NEXT(D_) do { if (q.cnt == 8) { int b_ = 0; if (F.lane == 0) b_ = (int)__hip_atomic_fetch_add(qctr, 8u, __ATOMIC_RELAXED, __HIP_MEMORY_SCOPE_AGENT); q.base = __builtin_amdgcn_readfirstlane(b_); q.cnt = 0; } \
;         D_ = decode_item(KA, F.ws, kind, q.base + q.cnt); ++q.cnt; } while (0)
; DI void item_scatter(const f32x4 (&v)[16], LAS float* scr, int lane) {
;     const int r4 = lane >> 4, c4 = lane & 15;
; #pragma unroll
;     for (int i = 0; i < 16; ++i) { const int k = 4 * i + r4;
; #pragma unroll
;         for (int j = 0; j < 4; ++j) scr[(4 * c4 + j) * 64 + (k ^ (4 * (c4 ^ j)))] = v[i][j]; }
;     LDS_WAIT(); asm volatile("" ::: "memory");
; }
; DI void run_items1(Frame& F, int kind, int quota, QState& q) {
;     ...
;     for (int n = 1; ; ++n) {
;         item_scatter(v, scr, F.lane);
;         TItem dn; dn.valid = false;
;         if (quota < 0 || n < quota) { RI_NEXT(dn); if (dn.valid) item_load(dn, v, F.lane); }
.LBB0_430:
	s_waitcnt vmcnt(0)
	ds_write_b32 v93, v2
	ds_write_b32 v94, v3 offset:256
	ds_write_b32 v95, v4 offset:512
	ds_write_b32 v96, v5 offset:768
	ds_write_b32 v97, v6
	ds_write_b32 v98, v7 offset:256
	ds_write_b32 v99, v8 offset:512
	ds_write_b32 v100, v9 offset:768
	ds_write_b32 v101, v10
	ds_write_b32 v102, v11 offset:256
	ds_write_b32 v103, v12 offset:512
	ds_write_b32 v104, v13 offset:768
	ds_write_b32 v105, v14
	ds_write_b32 v106, v15 offset:256
	ds_write_b32 v107, v16 offset:512
	ds_write_b32 v108, v17 offset:768
	ds_write_b32 v109, v18
	ds_write_b32 v110, v19 offset:256
	ds_write_b32 v111, v20 offset:512
	ds_write_b32 v112, v21 offset:768
	ds_write_b32 v113, v22
	ds_write_b32 v114, v23 offset:256
	ds_write_b32 v115, v24 offset:512
	ds_write_b32 v116, v25 offset:768
	ds_write_b32 v117, v26
	ds_write_b32 v118, v27 offset:256
	ds_write_b32 v119, v28 offset:512
	ds_write_b32 v120, v29 offset:768
	ds_write_b32 v121, v30
	ds_write_b32 v122, v31 offset:256
	ds_write_b32 v123, v32 offset:512
	ds_write_b32 v124, v33 offset:768
	ds_write_b32 v125, v34
	ds_write_b32 v126, v35 offset:256
	ds_write_b32 v127, v36 offset:512
	ds_write_b32 v128, v37 offset:768
	ds_write_b32 v129, v38
	ds_write_b32 v130, v39 offset:256
	ds_write_b32 v131, v40 offset:512
	ds_write_b32 v132, v41 offset:768
	ds_write_b32 v133, v42
	ds_write_b32 v134, v43 offset:256
	ds_write_b32 v135, v44 offset:512
	ds_write_b32 v136, v45 offset:768
	ds_write_b32 v137, v46
	ds_write_b32 v138, v47 offset:256
	ds_write_b32 v139, v48 offset:512
	ds_write_b32 v140, v49 offset:768
	ds_write_b32 v141, v50
	ds_write_b32 v142, v51 offset:256
	ds_write_b32 v143, v52 offset:512
	ds_write_b32 v144, v53 offset:768
	ds_write_b32 v145, v54
	ds_write_b32 v146, v55 offset:256
	ds_write_b32 v147, v56 offset:512
	ds_write_b32 v148, v57 offset:768
	ds_write_b32 v149, v58
	ds_write_b32 v150, v59 offset:256
	ds_write_b32 v151, v60 offset:512
	ds_write_b32 v152, v61 offset:768
	ds_write_b32 v153, v62
	ds_write_b32 v154, v63 offset:256
	ds_write_b32 v155, v64 offset:512
	ds_write_b32 v156, v65 offset:768
	s_waitcnt lgkmcnt(0)
	s_cmp_gt_u32 s38, 3
	s_mov_b64 s[2:3], 0
	s_cbranch_scc1 .LBB0_465
	s_cmp_lg_u32 s63, 4
	s_cbranch_scc1 .LBB0_437
	v_mov_b32_e32 v0, 0
	s_and_saveexec_b64 s[2:3], s[4:5]
	s_cbranch_execz .LBB0_436
	s_mov_b64 s[18:19], exec
	v_mbcnt_lo_u32_b32 v0, s18, 0
	v_mbcnt_hi_u32_b32 v0, s19, v0
	v_cmp_eq_u32_e32 vcc, 0, v0
	s_and_saveexec_b64 s[16:17], vcc
	s_cbranch_execz .LBB0_435
	s_bcnt1_i32_b64 s0, s[18:19]
	s_lshl_b32 s0, s0, 2
	v_mov_b32_e32 v66, s0
	global_atomic_add v66, v1, v66, s[12:13] sc0

; #define LAS __attribute__((address_space(3)))
; #define LDS_WAIT() asm volatile("s_waitcnt lgkmcnt(0)" ::: "memory")
; #define RI_NEXT(D_) do { if (q.cnt == 8) { int b_ = 0; if (F.lane == 0) b_ = (int)__hip_atomic_fetch_add(qctr, 8u, __ATOMIC_RELAXED, __HIP_MEMORY_SCOPE_AGENT); q.base = __builtin_amdgcn_readfirstlane(b_); q.cnt = 0; } \
;         D_ = decode_item(KA, F.ws, kind, q.base + q.cnt); ++q.cnt; } while (0)
; DI void item_scatter(const f32x4 (&v)[16], LAS float* scr, int lane) {
;     const int r4 = lane >> 4, c4 = lane & 15;
; #pragma unroll
;     for (int i = 0; i < 16; ++i) { const int k = 4 * i + r4;
; #pragma unroll
;         for (int j = 0; j < 4; ++j) scr[(4 * c4 + j) * 64 + (k ^ (4 * (c4 ^ j)))] = v[i][j]; }
;     LDS_WAIT(); asm volatile("" ::: "memory");
; }
; DI void run_items1(Frame& F, int kind, int quota, QState& q) {
;     ...
;     for (int n = 1; ; ++n) {
;         item_scatter(v, scr, F.lane);
;         TItem dn; dn.valid = false;
;         if (quota < 0 || n < quota) { RI_NEXT(dn); if (dn.valid) item_load(dn, v, F.lane); }
.LBB0_602:
	s_waitcnt vmcnt(15)
	ds_write_b32 v93, v2
	ds_write_b32 v94, v3 offset:256
	ds_write_b32 v95, v4 offset:512
	ds_write_b32 v96, v5 offset:768
	s_waitcnt vmcnt(14)
	ds_write_b32 v97, v6
	ds_write_b32 v98, v7 offset:256
	ds_write_b32 v99, v8 offset:512
	ds_write_b32 v100, v9 offset:768
	s_waitcnt vmcnt(13)
	ds_write_b32 v101, v10
	ds_write_b32 v102, v11 offset:256
	ds_write_b32 v103, v12 offset:512
	ds_write_b32 v104, v13 offset:768
	s_waitcnt vmcnt(12)
	ds_write_b32 v105, v14
	ds_write_b32 v106, v15 offset:256
	ds_write_b32 v107, v16 offset:512
	ds_write_b32 v108, v17 offset:768
	s_waitcnt vmcnt(11)
	ds_write_b32 v109, v18
	ds_write_b32 v110, v19 offset:256
	ds_write_b32 v111, v20 offset:512
	ds_write_b32 v112, v21 offset:768
	s_waitcnt vmcnt(10)
	ds_write_b32 v113, v22
	ds_write_b32 v114, v23 offset:256
	ds_write_b32 v115, v24 offset:512
	ds_write_b32 v116, v25 offset:768
	s_waitcnt vmcnt(9)
	ds_write_b32 v117, v26
	ds_write_b32 v118, v27 offset:256
	ds_write_b32 v119, v28 offset:512
	ds_write_b32 v120, v29 offset:768
	s_waitcnt vmcnt(8)
	ds_write_b32 v121, v30
	ds_write_b32 v122, v31 offset:256
	ds_write_b32 v123, v32 offset:512
	ds_write_b32 v124, v33 offset:768
	s_waitcnt vmcnt(7)
	ds_write_b32 v125, v34
	ds_write_b32 v126, v35 offset:256
	ds_write_b32 v127, v36 offset:512
	ds_write_b32 v128, v37 offset:768
	s_waitcnt vmcnt(6)
	ds_write_b32 v129, v38
	ds_write_b32 v130, v39 offset:256
	ds_write_b32 v131, v40 offset:512
	ds_write_b32 v132, v41 offset:768
	s_waitcnt vmcnt(5)
	ds_write_b32 v133, v42
	ds_write_b32 v134, v43 offset:256
	ds_write_b32 v135, v44 offset:512
	ds_write_b32 v136, v45 offset:768
	s_waitcnt vmcnt(4)
	ds_write_b32 v137, v46
	ds_write_b32 v138, v47 offset:256
	ds_write_b32 v139, v48 offset:512
	ds_write_b32 v140, v49 offset:768
	s_waitcnt vmcnt(3)
	ds_write_b32 v141, v50
	ds_write_b32 v142, v51 offset:256
	ds_write_b32 v143, v52 offset:512
	ds_write_b32 v144, v53 offset:768
	s_waitcnt vmcnt(2)
	ds_write_b32 v145, v54
	ds_write_b32 v146, v55 offset:256
	ds_write_b32 v147, v56 offset:512
	ds_write_b32 v148, v57 offset:768
	s_waitcnt vmcnt(1)
	ds_write_b32 v149, v58
	ds_write_b32 v150, v59 offset:256
	ds_write_b32 v151, v60 offset:512
	ds_write_b32 v152, v61 offset:768
	s_waitcnt vmcnt(0)
	ds_write_b32 v153, v62
	ds_write_b32 v154, v63 offset:256
	ds_write_b32 v155, v64 offset:512
	ds_write_b32 v156, v65 offset:768
	s_waitcnt lgkmcnt(0)
	s_cmp_gt_u32 s38, 3
	s_mov_b64 s[2:3], 0
	s_cbranch_scc1 .LBB0_637
	s_cmp_lg_u32 s63, 4
	s_cbranch_scc1 .LBB0_609
	v_mov_b32_e32 v0, 0
	s_and_saveexec_b64 s[2:3], s[4:5]
	s_cbranch_execz .LBB0_608
	s_mov_b64 s[18:19], exec
	v_mbcnt_lo_u32_b32 v0, s18, 0
	v_mbcnt_hi_u32_b32 v0, s19, v0
	v_cmp_eq_u32_e32 vcc, 0, v0
	s_and_saveexec_b64 s[16:17], vcc
	s_cbranch_execz .LBB0_607
	s_bcnt1_i32_b64 s0, s[18:19]
	s_lshl_b32 s0, s0, 2
	v_mov_b32_e32 v66, s0
	global_atomic_add v66, v1, v66, s[12:13] sc0
